# row pass 2: slot indices of row r+2 fetched one iteration ahead (no index round trip at the top of each row)
# speedup vs baseline: 1.0063x; 1.0010x over previous
; #define INP(k) inp_ptr(k)
; template <int MODE, bool FIRSTX>
; __device__ __forceinline__ void row_pass(Frame& F, int layer, bool final_out, int row0) {
;     const float* MOD = (const float*)(F.ws + WS_MOD);
;     bf16_t* X = (bf16_t*)(F.ws + WS_X); bf16_t* H = (bf16_t*)(F.ws + WS_H);
;     const bf16_t* Y = (const bf16_t*)(F.ws + WS_Y); const bf16_t* YK = (const bf16_t*)(F.ws + WS_R1 + R1_YK); const int* TS = (const int*)(F.ws + WS_SLOTDST);
;     const int rpw = (TALL - row0 + F.NGW - 1) / F.NGW;
;     const int r0 = row0 + F.gw * rpw, r1 = (r0 + rpw < TALL) ? r0 + rpw : TALL;
;     const int sub = (MODE == 2) ? 1 : 0;
;     const int gate_i = (MODE == 2) ? 5 : 2;
;     const int nlayer = (MODE == 2) ? layer + 1 : layer;
;     const int sh_i = (MODE == 1) ? 3 : 0, sc_i = (MODE == 1) ? 4 : 1;
;     const int lc = 8 * F.lane;
;     ...
;     f32x4 lg[4], lb[4], gt[4], sh[4], sc[4];
;     if (MODE != 0) {
; #pragma unroll
;         for (int q = 0; q < 4; ++q) { lg[q] = *(const f32x4*)(INP(IN_LNG) + (layer * 2 + sub) * 1024 + RP_COL(q)); lb[q] = *(const f32x4*)(INP(IN_LNB) + (layer * 2 + sub) * 1024 + RP_COL(q)); } }
;     constexpr int NY = (MODE == 2) ? 4 : (MODE == 1 ? 1 : 0);
;     f32x4 xf[4], xfn[4]; u32x4 xb[2], xbn[2]; u32x4 yb[NY ? NY : 1][2], ybn[NY ? NY : 1][2];
;     ...
;     if (r0 < r1) RP_LOAD(r0, xf, xb, yb);
.LBB0_1198:
	s_or_b64 exec, exec, s[2:3]
	s_mov_b32 s0, s53
	s_mov_b32 s29, s90
	s_mov_b32 s38, s73
	s_waitcnt lgkmcnt(0)
	s_barrier
	v_mbcnt_lo_u32_b32 v34, -1, 0
	v_mbcnt_hi_u32_b32 v34, -1, v34
	s_lshl_b32 s1, s38, 3
	s_add_i32 s3, s1, s0
	v_readlane_b32 s0, v232, 24
	s_lshl_b32 s2, s29, 3
	v_readlane_b32 s1, v232, 25
	s_and_b64 s[0:1], s[0:1], exec
	s_mov_b32 s0, 0xffff
	s_cselect_b32 s0, 0x107ff, s0
	s_abs_i32 s1, s2
	v_cvt_f32_u32_e32 v0, s1
	s_sub_i32 s4, 0, s1
	s_add_i32 s0, s0, s2
	s_xor_b32 s2, s0, s2
	v_rcp_iflag_f32_e32 v0, v0
	s_abs_i32 s0, s0
	s_ashr_i32 s2, s2, 31
	s_mov_b64 s[94:95], s[74:75]
	v_mul_f32_e32 v0, 0x4f7ffffe, v0
	v_cvt_u32_f32_e32 v0, v0
	s_nop 0
	v_readfirstlane_b32 s5, v0
	s_mul_i32 s4, s4, s5
	s_mul_hi_u32 s4, s5, s4
	s_add_i32 s5, s5, s4
	s_mul_hi_u32 s4, s0, s5
	s_mul_i32 s5, s4, s1
	s_sub_i32 s0, s0, s5
	s_add_i32 s5, s4, 1
	s_sub_i32 s6, s0, s1
	s_cmp_ge_u32 s0, s1
	s_cselect_b32 s4, s5, s4
	s_cselect_b32 s0, s6, s0
	s_add_i32 s5, s4, 1
	s_cmp_ge_u32 s0, s1
	s_cselect_b32 s0, s5, s4
	s_xor_b32 s0, s0, s2
	s_sub_i32 s0, s0, s2
	s_mul_i32 s1, s3, s0
	v_readlane_b32 s2, v232, 22
	s_add_i32 s26, s1, s2
	s_add_i32 s0, s26, s0
	s_min_i32 s10, s0, 0x10800
	s_mov_b64 s[0:1], s[88:89]
	s_load_dwordx2 s[2:3], s[0:1], 0x30
	s_lshl_b32 s0, s37, 11
	s_or_b32 s18, s0, 0x400
	v_lshlrev_b32_e32 v0, 3, v34
	s_lshl_b64 s[0:1], s[18:19], 2
	v_and_b32_e32 v0, 0x1f8, v0
	s_waitcnt lgkmcnt(0)
	s_add_u32 s2, s2, s0
	s_addc_u32 s3, s3, s1
	s_waitcnt vmcnt(0)
	v_lshlrev_b32_e32 v26, 2, v0
	global_load_dwordx4 v[2:5], v26, s[2:3]
	s_mov_b64 s[2:3], s[88:89]
	s_load_dwordx2 s[2:3], s[2:3], 0x38
	s_waitcnt lgkmcnt(0)
	s_add_u32 s2, s2, s0
	s_addc_u32 s3, s3, s1
	global_load_dwordx4 v[6:9], v26, s[2:3]
	s_mov_b64 s[2:3], s[88:89]
	s_load_dwordx2 s[2:3], s[2:3], 0x30
	s_waitcnt lgkmcnt(0)
	s_add_u32 s2, s2, s0
	s_addc_u32 s3, s3, s1
	global_load_dwordx4 v[10:13], v26, s[2:3] offset:16
	s_mov_b64 s[2:3], s[88:89]
	s_load_dwordx2 s[2:3], s[2:3], 0x38
	s_waitcnt lgkmcnt(0)
	s_add_u32 s2, s2, s0
	s_addc_u32 s3, s3, s1
	global_load_dwordx4 v[14:17], v26, s[2:3] offset:16
	s_mov_b64 s[2:3], s[88:89]
	s_load_dwordx2 s[2:3], s[2:3], 0x30
	s_waitcnt lgkmcnt(0)
	s_add_u32 s2, s2, s0
	s_addc_u32 s3, s3, s1
	global_load_dwordx4 v[18:21], v26, s[2:3] offset:2048
	s_mov_b64 s[2:3], s[88:89]
	s_load_dwordx2 s[2:3], s[2:3], 0x38
	s_waitcnt lgkmcnt(0)
	s_add_u32 s2, s2, s0
	s_addc_u32 s3, s3, s1
	global_load_dwordx4 v[22:25], v26, s[2:3] offset:2048
	s_mov_b64 s[2:3], s[88:89]
	s_load_dwordx2 s[2:3], s[2:3], 0x30
	s_waitcnt lgkmcnt(0)
	s_add_u32 s2, s2, s0
	s_addc_u32 s3, s3, s1
	global_load_dwordx4 v[26:29], v26, s[2:3] offset:2064
	s_mov_b64 s[2:3], s[88:89]
	s_cmp_ge_i32 s26, s10
	s_cbranch_scc1 .LBB0_1227
	s_load_dwordx2 s[2:3], s[2:3], 0x38
	v_lshlrev_b32_e32 v112, 2, v0
	v_lshlrev_b32_e32 v36, 1, v0
	v_mov_b32_e32 v37, v1
	s_mov_b64 s[4:5], 0x67800000
	s_waitcnt lgkmcnt(0)
	s_add_u32 s0, s2, s0
	s_addc_u32 s1, s3, s1
	s_add_u32 s11, s94, 0x100000
	s_addc_u32 s16, s95, 0
	s_ashr_i32 s27, s26, 31
	s_lshl_b64 s[2:3], s[26:27], 11
	global_load_dwordx4 v[30:33], v112, s[0:1] offset:2064
	s_add_u32 s0, s94, s2
	s_addc_u32 s1, s95, s3
	v_lshl_add_u64 v[36:37], s[0:1], 0, v[36:37]
	s_mov_b64 s[0:1], 0x34400000
	v_lshl_add_u64 v[38:39], v[36:37], 0, s[0:1]
	v_add_co_u32_e32 v36, vcc, s39, v36
	s_lshl_b64 s[6:7], s[26:27], 4
	s_nop 0
	v_addc_co_u32_e32 v37, vcc, 0, v37, vcc
	s_add_u32 s0, s94, s6
	global_load_dwordx4 v[94:97], v[36:37], off
	global_load_dwordx4 v[90:93], v[38:39], off offset:1024
	s_addc_u32 s1, s95, s7
	v_lshl_add_u64 v[36:37], s[94:95], 0, v[0:1]
	v_lshl_add_u64 v[114:115], v[36:37], 0, s[4:5]
	global_load_dwordx4 v[36:39], v191, s[0:1]
	global_load_dwordx4 v[200:203], v191, s[0:1] offset:16
	s_mul_i32 s0, s37, 0xaaaaaaab
	s_add_i32 s0, s0, 0x55555555
	s_cmp_gt_u32 s0, 0x55555554
	v_mov_b32_e32 v113, v1
	s_cselect_b64 s[74:75], -1, 0
	v_and_b32_e32 v34, 63, v34
	s_lshl_b64 s[0:1], s[26:27], 10
	v_or_b32_e32 v106, 4, v0
	v_or_b32_e32 v108, 0x200, v0
	v_or_b32_e32 v110, 0x204, v0
	v_lshl_add_u64 v[116:117], s[92:93], 0, v[112:113]
	v_lshl_or_b32 v118, v34, 4, s2
	v_mov_b32_e32 v119, s3
	v_mov_b32_e32 v121, s1
	v_or_b32_e32 v120, s0, v0
	s_mov_b32 s8, -1
	s_waitcnt vmcnt(0)
	v_ashrrev_i32_e32 v41, 31, v36
	v_mov_b32_e32 v40, v36
	v_ashrrev_i32_e32 v43, 31, v37
	v_mov_b32_e32 v42, v37
	v_lshlrev_b64 v[36:37], 10, v[42:43]
	v_lshlrev_b64 v[40:41], 10, v[40:41]
	v_lshl_add_u64 v[40:41], v[114:115], 0, v[40:41]
	v_lshl_add_u64 v[36:37], v[114:115], 0, v[36:37]
	global_load_dwordx2 v[142:143], v[40:41], off
	global_load_dwordx2 v[100:101], v[40:41], off offset:512
	global_load_dwordx2 v[140:141], v[36:37], off
	global_load_dwordx2 v[98:99], v[36:37], off offset:512
	v_ashrrev_i32_e32 v37, 31, v38
	v_mov_b32_e32 v36, v38
	v_ashrrev_i32_e32 v41, 31, v39
	v_mov_b32_e32 v40, v39
	v_lshlrev_b64 v[36:37], 10, v[36:37]
	v_lshlrev_b64 v[38:39], 10, v[40:41]
	v_lshl_add_u64 v[36:37], v[114:115], 0, v[36:37]
	global_load_dwordx2 v[144:145], v[36:37], off
	global_load_dwordx2 v[102:103], v[36:37], off offset:512
	v_lshl_add_u64 v[36:37], v[114:115], 0, v[38:39]
	global_load_dwordx2 v[148:149], v[36:37], off
	global_load_dwordx2 v[104:105], v[36:37], off offset:512
	s_branch .LBB0_1201

; template <int MODE, bool FIRSTX>
; __device__ __forceinline__ void row_pass(Frame& F, int layer, bool final_out, int row0) {
;     ...
;     if (r0 < r1) RP_LOAD(r0, xf, xb, yb);
;     int curm = -1;
;     for (int row = r0; row < r1; ++row) {
;         if (row + 1 < r1) RP_LOAD(row + 1, xfn, xbn, ybn);
.LBB0_1201:
	s_add_i32 s17, s26, 1
	s_cmp_ge_i32 s17, s10
	s_cselect_b64 s[60:61], -1, 0
	s_and_b64 vcc, exec, s[60:61]
	v_lshl_add_u64 v[138:139], s[94:95], 0, v[118:119]
	s_cbranch_vccnz .LBB0_1203
	s_add_u32 s0, s94, s6
	s_addc_u32 s1, s95, s7
	v_add_co_u32_e32 v122, vcc, 0x34400000, v138
	s_nop 1
	v_addc_co_u32_e32 v123, vcc, 0, v139, vcc
	global_load_dwordx4 v[66:69], v[122:123], off offset:2048
	v_ashrrev_i32_e32 v125, 31, v200
	v_mov_b32_e32 v124, v200
	v_ashrrev_i32_e32 v127, 31, v201
	v_mov_b32_e32 v126, v201
	v_ashrrev_i32_e32 v83, 31, v202
	v_mov_b32_e32 v82, v202
	v_ashrrev_i32_e32 v129, 31, v203
	v_mov_b32_e32 v128, v203
	v_lshlrev_b64 v[84:85], 10, v[126:127]
	v_lshlrev_b64 v[124:125], 10, v[124:125]
	v_lshlrev_b64 v[126:127], 10, v[128:129]
	v_lshlrev_b64 v[82:83], 10, v[82:83]
	v_lshl_add_u64 v[124:125], v[114:115], 0, v[124:125]
	v_lshl_add_u64 v[128:129], v[114:115], 0, v[84:85]
	v_lshl_add_u64 v[150:151], v[114:115], 0, v[82:83]
	v_lshl_add_u64 v[152:153], v[114:115], 0, v[126:127]
	global_load_dwordx4 v[82:85], v[122:123], off offset:3072
	global_load_dwordx2 v[136:137], v[124:125], off
	global_load_dwordx2 v[134:135], v[124:125], off offset:512
	global_load_dwordx2 v[132:133], v[128:129], off
	global_load_dwordx2 v[130:131], v[128:129], off offset:512
	s_nop 0
	global_load_dwordx2 v[128:129], v[150:151], off
	global_load_dwordx2 v[126:127], v[150:151], off offset:512
	global_load_dwordx2 v[124:125], v[152:153], off
	global_load_dwordx2 v[122:123], v[152:153], off offset:512
	global_load_dwordx4 v[200:203], v191, s[0:1] offset:32
